# DIFF loop: even/odd partial row sums (no back-to-back dependent adds)
# speedup vs baseline: 1.0070x; 1.0070x over previous
.LBB0_952:
	s_lshr_b32 s11, s19, 3
	s_and_b32 s10, s19, 31
	s_and_b32 s11, s11, 0xffffe0
	s_or_b32 s10, s11, s10
	s_bfe_u32 s25, s19, 0x10007
	s_lshl_b32 s10, s10, 8
	s_bfe_u32 s26, s19, 0x20005
	s_lshl_b32 s11, s25, 14
	s_ashr_i32 s20, s10, 31
	s_add_u32 s10, s10, s11
	s_addc_u32 s11, s20, 0
	s_lshl_b64 s[20:21], s[10:11], 9
	s_add_u32 s22, s12, s20
	s_addc_u32 s21, s13, s21
	s_lshl_b32 s20, s26, 6
	s_lshl_b32 s23, s26, 7
	s_add_u32 s22, s22, s23
	s_addc_u32 s23, s21, 0
	s_lshl_b32 s21, s25, 2
	s_or_b32 s21, s21, s26
	s_mul_i32 s21, s21, 0x208000
	s_add_u32 s25, s14, s21
	s_addc_u32 s26, s15, 0
	v_mov_b32_e32 v4, v230
	s_add_u32 s27, s16, s21
	s_addc_u32 s28, s17, 0
	v_readfirstlane_b32 s21, v4
	v_and_b32_e32 v18, 31, v4
	s_ashr_i32 s21, s21, 6
	s_cmp_lt_i32 s21, 8
	v_lshl_or_b32 v0, s21, 5, v18
	v_ashrrev_i32_e32 v2, 31, v0
	s_cselect_b64 vcc, -1, 0
	v_cndmask_b32_e32 v3, 0, v2, vcc
	v_cndmask_b32_e32 v2, v18, v0, vcc
	v_bfe_u32 v5, v4, 5, 1
	v_lshlrev_b64 v[2:3], 9, v[2:3]
	v_lshl_add_u64 v[2:3], s[22:23], 0, v[2:3]
	v_lshlrev_b32_e32 v0, 4, v5
	v_lshl_add_u64 v[2:3], v[2:3], 0, v[0:1]
	global_load_dwordx4 v[130:133], v[2:3], off
	global_load_dwordx4 v[134:137], v[2:3], off offset:64
	global_load_dwordx4 v[138:141], v[2:3], off offset:32
	global_load_dwordx4 v[142:145], v[2:3], off offset:96
	s_lshl_b32 s29, s21, 10
	s_ashr_i32 s30, s29, 31
	v_and_b32_e32 v0, 63, v4
	v_and_b32_e32 v2, 19, v4
	v_lshlrev_b32_e32 v3, 1, v4
	v_lshrrev_b32_e32 v4, 1, v4
	s_add_u32 s22, s25, s29
	v_and_b32_e32 v3, 8, v3
	v_and_b32_e32 v4, 4, v4
	s_addc_u32 s23, s26, s30
	s_add_i32 s21, s29, 0
	v_lshlrev_b32_e32 v19, 10, v5
	v_or3_b32 v2, v2, v3, v4
	v_lshlrev_b32_e32 v0, 4, v0
	s_add_u32 s26, s27, s29
	s_mov_b32 m0, s21
	v_lshl_or_b32 v2, v2, 4, v19
	v_lshl_add_u64 v[174:175], s[22:23], 0, v[0:1]
	global_load_lds_dwordx4 v0, s[22:23]
	s_addc_u32 s27, s28, s30
	s_add_i32 m0, s21, 0x2000
	s_mov_b64 s[22:23], 0x2000
	v_add_u32_e32 v188, 0, v2
	v_lshl_add_u64 v[176:177], s[26:27], 0, v[0:1]
	global_load_lds_dwordx4 v0, s[26:27]
	v_lshl_add_u64 v[2:3], v[174:175], 0, s[22:23]
	s_add_i32 m0, s21, 0x4000
	v_mov_b32_e32 v150, v1
	global_load_lds_dwordx4 v[2:3], off
	v_lshl_add_u64 v[2:3], v[176:177], 0, s[22:23]
	s_add_i32 m0, s21, 0x6000
	v_lshl_or_b32 v0, v18, 4, v19
	global_load_lds_dwordx4 v[2:3], off
	s_waitcnt vmcnt(0)
	s_waitcnt vmcnt(0) lgkmcnt(0)
	s_barrier
	ds_read_b128 v[2:5], v188
	ds_read_b128 v[6:9], v188 offset:4096
	ds_read_b128 v[98:101], v188 offset:512
	ds_read_b128 v[10:13], v188 offset:2048
	ds_read_b128 v[102:105], v188 offset:4608
	ds_read_b128 v[14:17], v188 offset:6144
	ds_read_b128 v[162:165], v188 offset:2560
	ds_read_b128 v[166:169], v188 offset:6656
	s_mov_b32 s22, 2
	s_mov_b32 s23, 1
	s_mov_b32 s27, 0
	s_mov_b32 s25, 0
	s_mov_b32 s26, 0
	v_add_u32_e32 v0, 0, v0
	v_mov_b32_e32 v151, v150
	v_mov_b32_e32 v152, v150
	v_mov_b32_e32 v153, v150
	v_mov_b32_e32 v154, v150
	v_mov_b32_e32 v155, v150
	v_mov_b32_e32 v156, v150
	v_mov_b32_e32 v157, v150
	s_waitcnt lgkmcnt(7)
	v_mfma_f32_32x32x16_bf16 v[82:97], v[2:5], v[130:133], 0
	v_mov_b32_e32 v2, 0
	v_mov_b32_e32 v3, v2
	v_mov_b32_e32 v4, v2
	v_mov_b32_e32 v5, v2
	v_mov_b32_e32 v18, v2
	v_mov_b32_e32 v19, v2
	v_mov_b32_e32 v20, v2
	s_waitcnt lgkmcnt(6)
	v_mfma_f32_32x32x16_bf16 v[66:81], v[6:9], v[134:137], 0
	v_mov_b32_e32 v6, v2
	v_mov_b32_e32 v7, v2
	v_mov_b32_e32 v8, v2
	v_mov_b32_e32 v9, v2
	v_mov_b32_e32 v21, v2
	v_mov_b32_e32 v22, v2
	v_mov_b32_e32 v23, v2
	s_waitcnt lgkmcnt(4)
	v_mfma_f32_32x32x16_bf16 v[82:97], v[10:13], v[138:141], v[82:97]
	v_mov_b32_e32 v10, v2
	v_mov_b32_e32 v11, v2
	v_mov_b32_e32 v12, v2
	v_mov_b32_e32 v13, v2
	v_mov_b32_e32 v24, v2
	v_mov_b32_e32 v25, v2
	v_mov_b32_e32 v26, v2
	s_waitcnt lgkmcnt(2)
	v_mfma_f32_32x32x16_bf16 v[66:81], v[14:17], v[142:145], v[66:81]
	v_mov_b32_e32 v14, v2
	v_mov_b32_e32 v15, v2
	v_mov_b32_e32 v16, v2
	v_mov_b32_e32 v17, v2
	v_mov_b32_e32 v27, v2
	v_mov_b32_e32 v28, v2
	v_mov_b32_e32 v29, v2
	v_mov_b32_e32 v30, v2
	v_mov_b32_e32 v31, v2
	v_mov_b32_e32 v32, v2
	v_mov_b32_e32 v33, v2
	v_mov_b32_e32 v158, v150
	v_mov_b32_e32 v159, v150
	v_mov_b32_e32 v160, v150
	v_mov_b32_e32 v161, v150
	v_mov_b32_e32 v146, v150
	v_mov_b32_e32 v147, v150
	v_mov_b32_e32 v148, v150
	v_mov_b32_e32 v149, v150
	v_mov_b32_e32 v34, v2
	v_mov_b32_e32 v35, v2
	v_mov_b32_e32 v36, v2
	v_mov_b32_e32 v37, v2
	v_mov_b32_e32 v38, v2
	v_mov_b32_e32 v39, v2
	v_mov_b32_e32 v40, v2
	v_mov_b32_e32 v41, v2
	v_mov_b32_e32 v42, v2
	v_mov_b32_e32 v43, v2
	v_mov_b32_e32 v44, v2
	v_mov_b32_e32 v45, v2
	v_mov_b32_e32 v46, v2
	v_mov_b32_e32 v47, v2
	v_mov_b32_e32 v48, v2
	v_mov_b32_e32 v49, v2
	v_mov_b32_e32 v50, v2
	v_mov_b32_e32 v51, v2
	v_mov_b32_e32 v52, v2
	v_mov_b32_e32 v53, v2
	v_mov_b32_e32 v54, v2
	v_mov_b32_e32 v55, v2
	v_mov_b32_e32 v56, v2
	v_mov_b32_e32 v57, v2
	v_mov_b32_e32 v58, v2
	v_mov_b32_e32 v59, v2
	v_mov_b32_e32 v60, v2
	v_mov_b32_e32 v61, v2
	v_mov_b32_e32 v62, v2
	v_mov_b32_e32 v63, v2
	v_mov_b32_e32 v64, v2
	v_mov_b32_e32 v65, v2
	v_mov_b32_e32 v178, v2
	v_mov_b32_e32 v179, v2
	v_mov_b32_e32 v232, v178
	v_mov_b32_e32 v233, v179
	v_mov_b32_e32 v234, 0
	v_mov_b32_e32 v235, 0
.LBB0_953:
	v_mfma_f32_32x32x16_bf16 v[114:129], v[98:101], v[130:133], 0
	s_min_i32 s28, s26, 0x101
	s_lshl_b32 s28, s28, 13
	s_add_i32 s88, s28, 0x4000
	s_lshl_b32 s28, s22, 14
	s_add_i32 s28, s21, s28
	v_lshl_add_u64 v[106:107], v[174:175], 0, s[88:89]
	s_mov_b32 m0, s28
	v_lshl_add_u32 v181, s27, 14, v0
	global_load_lds_dwordx4 v[106:107], off
	v_lshl_add_u64 v[106:107], v[176:177], 0, s[88:89]
	s_add_i32 m0, s28, 0x2000
	s_lshl_b32 s28, s25, 14
	global_load_lds_dwordx4 v[106:107], off
	ds_read_b128 v[190:193], v181 offset:12288
	v_add_u32_e32 v189, s28, v0
	v_lshl_add_u32 v210, s23, 14, v188
	v_exp_f32_e32 v194, v82
	v_exp_f32_e32 v196, v83
	v_exp_f32_e32 v198, v84
	v_exp_f32_e32 v200, v85
	v_mfma_f32_32x32x16_bf16 v[98:113], v[102:105], v[134:137], 0
	ds_read_b128 v[82:85], v181 offset:12800
	v_cvt_pk_bf16_f32 v170, v194, v196
	v_add_f32_e32 v232, v194, v232
	v_add_f32_e32 v234, v196, v234
	v_cvt_pk_bf16_f32 v171, v198, v200
	v_add_f32_e32 v232, v198, v232
	v_add_f32_e32 v234, v200, v234
	v_exp_f32_e32 v202, v86
	v_exp_f32_e32 v204, v87
	s_waitcnt lgkmcnt(3)
	v_mfma_f32_32x32x16_bf16 v[114:129], v[162:165], v[138:141], v[114:129]
	v_cvt_pk_bf16_f32 v172, v202, v204
	v_add_f32_e32 v232, v202, v232
	v_add_f32_e32 v234, v204, v234
	v_exp_f32_e32 v206, v88
	v_exp_f32_e32 v208, v89
	s_waitcnt lgkmcnt(2)
	v_mfma_f32_32x32x16_bf16 v[98:113], v[166:169], v[142:145], v[98:113]
	v_exp_f32_e32 v168, v92
	v_exp_f32_e32 v166, v93
	v_cvt_pk_bf16_f32 v173, v206, v208
	v_add_f32_e32 v232, v206, v232
	v_add_f32_e32 v234, v208, v234
	v_exp_f32_e32 v214, v90
	v_exp_f32_e32 v216, v91
	s_waitcnt lgkmcnt(1)
	v_mfma_f32_32x32x16_bf16 v[34:49], v[190:193], v[150:153], v[34:49]
	ds_read_b128 v[86:89], v181 offset:14336
	v_cvt_pk_bf16_f32 v162, v214, v216
	v_add_f32_e32 v232, v214, v232
	v_add_f32_e32 v234, v216, v234
	v_cvt_pk_bf16_f32 v163, v168, v166
	v_add_f32_e32 v232, v168, v232
	v_add_f32_e32 v234, v166, v234
	v_exp_f32_e32 v182, v94
	v_exp_f32_e32 v180, v95
	s_waitcnt lgkmcnt(1)
	v_mfma_f32_32x32x16_bf16 v[50:65], v[82:85], v[150:153], v[50:65]
	ds_read_b128 v[90:93], v181 offset:14848
	v_cvt_pk_bf16_f32 v164, v182, v180
	v_add_f32_e32 v232, v182, v232
	v_add_f32_e32 v234, v180, v234
	v_exp_f32_e32 v186, v96
	v_exp_f32_e32 v184, v97
	v_mfma_f32_32x32x16_bf16 v[2:17], v[190:193], v[158:161], v[2:17]
	v_cvt_pk_bf16_f32 v165, v186, v184
	v_add_f32_e32 v232, v186, v232
	v_add_f32_e32 v234, v184, v234
	v_exp_f32_e32 v195, v66
	v_exp_f32_e32 v197, v67
	v_exp_f32_e32 v199, v68
	v_exp_f32_e32 v201, v69
	v_mfma_f32_32x32x16_bf16 v[18:33], v[82:85], v[158:161], v[18:33]
	v_cvt_pk_bf16_f32 v158, v195, v197
	v_add_f32_e32 v233, v195, v233
	v_add_f32_e32 v235, v197, v235
	v_cvt_pk_bf16_f32 v159, v199, v201
	v_add_f32_e32 v233, v199, v233
	v_add_f32_e32 v235, v201, v235
	v_exp_f32_e32 v203, v70
	v_exp_f32_e32 v205, v71
	s_waitcnt lgkmcnt(1)
	v_mfma_f32_32x32x16_bf16 v[34:49], v[86:89], v[154:157], v[34:49]
	ds_read_b128 v[66:69], v210
	v_cvt_pk_bf16_f32 v160, v203, v205
	v_add_f32_e32 v233, v203, v233
	v_add_f32_e32 v235, v205, v235
	v_exp_f32_e32 v207, v72
	v_exp_f32_e32 v209, v73
	s_waitcnt lgkmcnt(1)
	v_mfma_f32_32x32x16_bf16 v[50:65], v[90:93], v[154:157], v[50:65]
	ds_read_b128 v[70:73], v210 offset:4096
	v_exp_f32_e32 v169, v76
	v_exp_f32_e32 v167, v77
	v_cvt_pk_bf16_f32 v161, v207, v209
	v_add_f32_e32 v233, v207, v233
	v_add_f32_e32 v235, v209, v235
	v_exp_f32_e32 v215, v74
	v_exp_f32_e32 v217, v75
	v_mfma_f32_32x32x16_bf16 v[2:17], v[86:89], v[146:149], v[2:17]
	ds_read_b128 v[152:155], v210 offset:2048
	v_cvt_pk_bf16_f32 v190, v215, v217
	v_add_f32_e32 v233, v215, v233
	v_add_f32_e32 v235, v217, v235
	v_cvt_pk_bf16_f32 v191, v169, v167
	v_add_f32_e32 v233, v169, v233
	v_add_f32_e32 v235, v167, v235
	v_exp_f32_e32 v183, v78
	v_exp_f32_e32 v181, v79
	v_mfma_f32_32x32x16_bf16 v[18:33], v[90:93], v[146:149], v[18:33]
	v_exp_f32_e32 v187, v80
	v_exp_f32_e32 v185, v81
	ds_read_b128 v[194:197], v210 offset:6144
	v_cvt_pk_bf16_f32 v192, v183, v181
	v_add_f32_e32 v233, v183, v233
	v_add_f32_e32 v235, v181, v235
	v_cvt_pk_bf16_f32 v193, v187, v185
	v_add_f32_e32 v233, v187, v233
	v_add_f32_e32 v235, v185, v235
	s_waitcnt lgkmcnt(3)
	v_mfma_f32_32x32x16_bf16 v[82:97], v[66:69], v[130:133], 0
	ds_read_b128 v[146:149], v189 offset:8192
	v_exp_f32_e32 v198, v114
	v_exp_f32_e32 v200, v115
	v_exp_f32_e32 v202, v116
	v_exp_f32_e32 v204, v117
	s_waitcnt lgkmcnt(3)
	v_mfma_f32_32x32x16_bf16 v[66:81], v[70:73], v[134:137], 0
	ds_read_b128 v[114:117], v189 offset:8704
	v_cvt_pk_bf16_f32 v150, v198, v200
	v_add_f32_e32 v232, v198, v232
	v_add_f32_e32 v234, v200, v234
	v_cvt_pk_bf16_f32 v151, v202, v204
	v_add_f32_e32 v232, v202, v232
	v_add_f32_e32 v234, v204, v234
	v_exp_f32_e32 v206, v118
	v_exp_f32_e32 v208, v119
	s_waitcnt lgkmcnt(3)
	v_mfma_f32_32x32x16_bf16 v[82:97], v[152:155], v[138:141], v[82:97]
	v_cvt_pk_bf16_f32 v152, v206, v208
	v_add_f32_e32 v232, v206, v232
	v_add_f32_e32 v234, v208, v234
	v_exp_f32_e32 v214, v120
	v_exp_f32_e32 v216, v121
	s_waitcnt lgkmcnt(2)
	v_mfma_f32_32x32x16_bf16 v[66:81], v[194:197], v[142:145], v[66:81]
	v_cvt_pk_bf16_f32 v153, v214, v216
	v_add_f32_e32 v232, v214, v232
	v_add_f32_e32 v234, v216, v234
	v_exp_f32_e32 v194, v122
	v_exp_f32_e32 v196, v123
	v_exp_f32_e32 v218, v124
	v_exp_f32_e32 v220, v125
	s_waitcnt lgkmcnt(1)
	v_mfma_f32_32x32x16_bf16 v[34:49], v[146:149], v[170:173], v[34:49]
	ds_read_b128 v[118:121], v189 offset:10240
	v_cvt_pk_bf16_f32 v154, v194, v196
	v_add_f32_e32 v232, v194, v232
	v_add_f32_e32 v234, v196, v234
	v_cvt_pk_bf16_f32 v155, v218, v220
	v_add_f32_e32 v232, v218, v232
	v_add_f32_e32 v234, v220, v234
	v_exp_f32_e32 v126, v126
	v_exp_f32_e32 v222, v127
	s_waitcnt lgkmcnt(1)
	v_mfma_f32_32x32x16_bf16 v[50:65], v[114:117], v[170:173], v[50:65]
	ds_read_b128 v[122:125], v189 offset:10752
	v_cvt_pk_bf16_f32 v156, v126, v222
	v_add_f32_e32 v232, v126, v232
	v_add_f32_e32 v234, v222, v234
	v_exp_f32_e32 v128, v128
	v_exp_f32_e32 v170, v129
	v_mfma_f32_32x32x16_bf16 v[2:17], v[146:149], v[158:161], v[2:17]
	v_cvt_pk_bf16_f32 v157, v128, v170
	v_add_f32_e32 v232, v128, v232
	v_add_f32_e32 v234, v170, v234
	v_exp_f32_e32 v199, v98
	v_exp_f32_e32 v201, v99
	v_exp_f32_e32 v203, v100
	v_exp_f32_e32 v205, v101
	v_mfma_f32_32x32x16_bf16 v[18:33], v[114:117], v[158:161], v[18:33]
	v_cvt_pk_bf16_f32 v158, v199, v201
	v_add_f32_e32 v233, v199, v233
	v_add_f32_e32 v235, v201, v235
	v_cvt_pk_bf16_f32 v159, v203, v205
	v_add_f32_e32 v233, v203, v233
	v_add_f32_e32 v235, v205, v235
	v_exp_f32_e32 v207, v102
	v_exp_f32_e32 v209, v103
	s_waitcnt lgkmcnt(1)
	v_mfma_f32_32x32x16_bf16 v[34:49], v[118:121], v[162:165], v[34:49]
	ds_read_b128 v[98:101], v210 offset:512
	v_cvt_pk_bf16_f32 v160, v207, v209
	v_add_f32_e32 v233, v207, v233
	v_add_f32_e32 v235, v209, v235
	v_exp_f32_e32 v215, v104
	v_exp_f32_e32 v217, v105
	s_waitcnt lgkmcnt(1)
	v_mfma_f32_32x32x16_bf16 v[50:65], v[122:125], v[162:165], v[50:65]
	ds_read_b128 v[102:105], v210 offset:4608
	v_cvt_pk_bf16_f32 v161, v215, v217
	v_add_f32_e32 v233, v215, v233
	v_add_f32_e32 v235, v217, v235
	v_exp_f32_e32 v195, v106
	v_exp_f32_e32 v197, v107
	v_exp_f32_e32 v219, v108
	v_exp_f32_e32 v221, v109
	v_mfma_f32_32x32x16_bf16 v[2:17], v[118:121], v[190:193], v[2:17]
	ds_read_b128 v[162:165], v210 offset:2560
	v_cvt_pk_bf16_f32 v146, v195, v197
	v_add_f32_e32 v233, v195, v233
	v_add_f32_e32 v235, v197, v235
	v_cvt_pk_bf16_f32 v147, v219, v221
	v_add_f32_e32 v233, v219, v233
	v_add_f32_e32 v235, v221, v235
	v_exp_f32_e32 v127, v110
	v_exp_f32_e32 v223, v111
	v_mfma_f32_32x32x16_bf16 v[18:33], v[122:125], v[190:193], v[18:33]
	v_exp_f32_e32 v129, v112
	ds_read_b128 v[166:169], v210 offset:6656
	v_exp_f32_e32 v171, v113
	v_cvt_pk_bf16_f32 v148, v127, v223
	v_add_f32_e32 v233, v127, v233
	v_add_f32_e32 v235, v223, v235
	v_cvt_pk_bf16_f32 v149, v129, v171
	v_add_f32_e32 v233, v129, v233
	v_add_f32_e32 v235, v171, v235
	s_add_i32 s27, s22, 1
	s_waitcnt vmcnt(0)
	s_and_b32 s28, s27, 3
	s_add_i32 s26, s26, 1
	s_cmpk_eq_i32 s26, 0x104
	s_mov_b32 s27, s25
	s_mov_b32 s25, s23
	s_mov_b32 s23, s22
	s_mov_b32 s22, s28
	s_waitcnt vmcnt(0) lgkmcnt(0)
	s_barrier
	s_cbranch_scc0 .LBB0_953
	v_add_f32_e32 v178, v232, v234
	v_add_f32_e32 v179, v233, v235
	ds_read_b128 v[66:69], v189 offset:12288
	ds_read_b128 v[70:73], v189 offset:12800
	v_mov_b32_e32 v0, v230
	s_waitcnt lgkmcnt(1)
	v_mfma_f32_32x32x16_bf16 v[34:49], v[66:69], v[150:153], v[34:49]
	s_waitcnt lgkmcnt(0)
	v_mfma_f32_32x32x16_bf16 v[50:65], v[70:73], v[150:153], v[50:65]
	v_mfma_f32_32x32x16_bf16 v[2:17], v[66:69], v[158:161], v[2:17]
	v_mfma_f32_32x32x16_bf16 v[18:33], v[70:73], v[158:161], v[18:33]
	ds_read_b128 v[68:71], v189 offset:14336
	ds_read_b128 v[72:75], v189 offset:14848
	v_mbcnt_lo_u32_b32 v76, -1, 0
	v_mbcnt_hi_u32_b32 v76, -1, v76
	v_mbcnt_lo_u32_b32 v77, -1, 0
	v_mbcnt_hi_u32_b32 v77, -1, v77
	global_load_dwordx2 v[66:67], v1, s[6:7]
	v_lshlrev_b32_e32 v77, 2, v77
	v_xor_b32_e32 v77, 0x80, v77
	v_lshlrev_b32_e32 v76, 2, v76
	ds_bpermute_b32 v77, v77, v179
	v_xor_b32_e32 v76, 0x80, v76
	ds_bpermute_b32 v76, v76, v178
	s_waitcnt lgkmcnt(3)
	v_mfma_f32_32x32x16_bf16 v[2:17], v[68:71], v[146:149], v[2:17]
	v_readfirstlane_b32 s21, v0
	s_ashr_i32 s21, s21, 1
	s_andn2_b32 s21, s21, 31
	s_cmpk_lt_i32 s21, 0x100
	s_waitcnt lgkmcnt(2)
	v_mfma_f32_32x32x16_bf16 v[18:33], v[72:75], v[146:149], v[18:33]
	v_mfma_f32_32x32x16_bf16 v[34:49], v[68:71], v[154:157], v[34:49]
	s_waitcnt lgkmcnt(1)
	v_add_f32_e32 v70, v179, v77
	v_mbcnt_lo_u32_b32 v68, -1, 0
	v_mbcnt_hi_u32_b32 v68, -1, v68
	v_rcp_f32_e32 v70, v70
	v_lshlrev_b32_e32 v69, 2, v68
	s_waitcnt lgkmcnt(0)
	v_add_f32_e32 v68, v178, v76
	v_rcp_f32_e32 v68, v68
	s_waitcnt vmcnt(0)
	v_mul_f32_e32 v66, v66, v70
	v_mfma_f32_32x32x16_bf16 v[50:65], v[72:75], v[154:157], v[50:65]
	v_mul_f32_e64 v2, v2, v66
	v_mul_f32_e64 v3, v3, v66
	v_mul_f32_e64 v18, v18, v66
	v_mul_f32_e64 v19, v19, v66
	v_mul_f32_e64 v4, v4, v66
	v_mul_f32_e64 v5, v5, v66
	v_pk_mul_f32 v[20:21], v[20:21], v[66:67] op_sel_hi:[1,0]
	v_pk_mul_f32 v[70:71], v[24:25], v[66:67] op_sel_hi:[1,0]
	v_pk_fma_f32 v[24:25], v[34:35], v[68:69], v[2:3] op_sel_hi:[1,0,1] neg_lo:[0,0,1] neg_hi:[0,0,1]
	v_pk_mul_f32 v[72:73], v[26:27], v[66:67] op_sel_hi:[1,0]
	s_nop 1
	v_pk_fma_f32 v[2:3], v[50:51], v[68:69], v[18:19] op_sel_hi:[1,0,1] neg_lo:[0,0,1] neg_hi:[0,0,1]
	v_pk_fma_f32 v[26:27], v[36:37], v[68:69], v[4:5] op_sel_hi:[1,0,1] neg_lo:[0,0,1] neg_hi:[0,0,1]
	v_pk_fma_f32 v[4:5], v[52:53], v[68:69], v[20:21] op_sel_hi:[1,0,1] neg_lo:[0,0,1] neg_hi:[0,0,1]
	v_pk_mul_f32 v[18:19], v[2:3], v[2:3]
	v_pk_mul_f32 v[6:7], v[6:7], v[66:67] op_sel_hi:[1,0]
	v_pk_mul_f32 v[22:23], v[22:23], v[66:67] op_sel_hi:[1,0]
	v_pk_mul_f32 v[36:37], v[4:5], v[4:5]
	v_pk_fma_f32 v[18:19], v[24:25], v[24:25], v[18:19]
	v_pk_mul_f32 v[74:75], v[28:29], v[66:67] op_sel_hi:[1,0]
	v_pk_fma_f32 v[28:29], v[38:39], v[68:69], v[6:7] op_sel_hi:[1,0,1] neg_lo:[0,0,1] neg_hi:[0,0,1]
	v_pk_fma_f32 v[6:7], v[54:55], v[68:69], v[22:23] op_sel_hi:[1,0,1] neg_lo:[0,0,1] neg_hi:[0,0,1]
	v_pk_fma_f32 v[36:37], v[26:27], v[26:27], v[36:37]
	v_add_f32_e32 v18, v18, v19
	v_pk_mul_f32 v[8:9], v[8:9], v[66:67] op_sel_hi:[1,0]
	v_pk_mul_f32 v[38:39], v[6:7], v[6:7]
	v_add_f32_e32 v18, v36, v18
	v_pk_mul_f32 v[76:77], v[30:31], v[66:67] op_sel_hi:[1,0]
	v_pk_fma_f32 v[30:31], v[40:41], v[68:69], v[8:9] op_sel_hi:[1,0,1] neg_lo:[0,0,1] neg_hi:[0,0,1]
	v_pk_fma_f32 v[8:9], v[56:57], v[68:69], v[70:71] op_sel_hi:[1,0,1] neg_lo:[0,0,1] neg_hi:[0,0,1]
	v_pk_fma_f32 v[38:39], v[28:29], v[28:29], v[38:39]
	v_add_f32_e32 v18, v37, v18
	v_pk_mul_f32 v[10:11], v[10:11], v[66:67] op_sel_hi:[1,0]
	v_pk_mul_f32 v[40:41], v[8:9], v[8:9]
	v_add_f32_e32 v18, v38, v18
	v_pk_mul_f32 v[78:79], v[32:33], v[66:67] op_sel_hi:[1,0]
	v_pk_fma_f32 v[32:33], v[42:43], v[68:69], v[10:11] op_sel_hi:[1,0,1] neg_lo:[0,0,1] neg_hi:[0,0,1]
	v_pk_fma_f32 v[10:11], v[58:59], v[68:69], v[72:73] op_sel_hi:[1,0,1] neg_lo:[0,0,1] neg_hi:[0,0,1]
	v_pk_fma_f32 v[40:41], v[30:31], v[30:31], v[40:41]
	v_add_f32_e32 v18, v39, v18
	v_pk_mul_f32 v[12:13], v[12:13], v[66:67] op_sel_hi:[1,0]
	v_pk_mul_f32 v[42:43], v[10:11], v[10:11]
	v_add_f32_e32 v18, v40, v18
	v_pk_fma_f32 v[34:35], v[44:45], v[68:69], v[12:13] op_sel_hi:[1,0,1] neg_lo:[0,0,1] neg_hi:[0,0,1]
	v_pk_fma_f32 v[12:13], v[60:61], v[68:69], v[74:75] op_sel_hi:[1,0,1] neg_lo:[0,0,1] neg_hi:[0,0,1]
	v_pk_fma_f32 v[42:43], v[32:33], v[32:33], v[42:43]
	v_add_f32_e32 v18, v41, v18
	v_pk_mul_f32 v[14:15], v[14:15], v[66:67] op_sel_hi:[1,0]
	v_pk_mul_f32 v[44:45], v[12:13], v[12:13]
	v_add_f32_e32 v18, v42, v18
	v_pk_fma_f32 v[20:21], v[46:47], v[68:69], v[14:15] op_sel_hi:[1,0,1] neg_lo:[0,0,1] neg_hi:[0,0,1]
	v_pk_fma_f32 v[14:15], v[62:63], v[68:69], v[76:77] op_sel_hi:[1,0,1] neg_lo:[0,0,1] neg_hi:[0,0,1]
	v_pk_fma_f32 v[44:45], v[34:35], v[34:35], v[44:45]
	v_add_f32_e32 v18, v43, v18
	v_pk_mul_f32 v[16:17], v[16:17], v[66:67] op_sel_hi:[1,0]
	v_pk_mul_f32 v[46:47], v[14:15], v[14:15]
	v_add_f32_e32 v18, v44, v18
	v_pk_fma_f32 v[22:23], v[48:49], v[68:69], v[16:17] op_sel_hi:[1,0,1] neg_lo:[0,0,1] neg_hi:[0,0,1]
	v_pk_fma_f32 v[16:17], v[64:65], v[68:69], v[78:79] op_sel_hi:[1,0,1] neg_lo:[0,0,1] neg_hi:[0,0,1]
	v_pk_fma_f32 v[46:47], v[20:21], v[20:21], v[46:47]
	v_add_f32_e32 v18, v45, v18
	v_pk_mul_f32 v[48:49], v[16:17], v[16:17]
	v_add_f32_e32 v18, v46, v18
	v_pk_fma_f32 v[48:49], v[22:23], v[22:23], v[48:49]
	v_add_f32_e32 v18, v47, v18
	v_add_f32_e32 v18, v48, v18
	v_add_f32_e32 v36, v49, v18
	v_xor_b32_e32 v18, 0x80, v69
	ds_bpermute_b32 v37, v18, v36
	s_cbranch_scc0 .LBB0_951
	s_waitcnt lgkmcnt(0)
	v_add_f32_e32 v36, v36, v37
	v_fmamk_f32 v36, v36, 0x3c800000, v224
	v_cmp_gt_f32_e32 vcc, s31, v36
	v_mul_f32_e32 v37, 0x4b800000, v36
	v_and_or_b32 v18, v0, 31, s21
	v_cndmask_b32_e32 v36, v36, v37, vcc
	v_rsq_f32_e32 v36, v36
	v_lshrrev_b32_e32 v0, 3, v0
	v_and_b32_e32 v0, 4, v0
	v_lshlrev_b32_e32 v41, 2, v0
	v_mul_f32_e32 v37, 0x45800000, v36
	v_cndmask_b32_e32 v36, v36, v37, vcc
	v_mul_f32_e32 v40, v67, v36
	global_load_dwordx4 v[36:39], v41, s[8:9] offset:128
	s_lshl_b64 s[10:11], s[10:11], 11
	s_add_u32 s10, s2, s10
	s_addc_u32 s11, s3, s11
	s_lshl_b32 s20, s20, 1
	s_add_u32 s10, s10, s20
	v_ashrrev_i32_e32 v19, 31, v18
	s_addc_u32 s11, s11, 0
	v_lshlrev_b64 v[18:19], 11, v[18:19]
	v_lshl_add_u64 v[18:19], s[10:11], 0, v[18:19]
	v_lshlrev_b32_e32 v0, 1, v0
	v_lshl_add_u64 v[18:19], v[18:19], 0, v[0:1]
	s_waitcnt vmcnt(0)
	v_pk_mul_f32 v[36:37], v[40:41], v[36:37] op_sel_hi:[0,1]
	v_pk_mul_f32 v[2:3], v[2:3], v[36:37]
	v_pk_mul_f32 v[36:37], v[40:41], v[38:39] op_sel_hi:[0,1]
	v_pk_mul_f32 v[4:5], v[4:5], v[36:37]
	global_load_dwordx4 v[36:39], v41, s[8:9] offset:160
	v_cvt_pk_bf16_f32 v2, v2, v3
	v_cvt_pk_bf16_f32 v3, v4, v5
	s_waitcnt vmcnt(0)
	v_pk_mul_f32 v[36:37], v[40:41], v[36:37] op_sel_hi:[0,1]
	v_pk_mul_f32 v[6:7], v[6:7], v[36:37]
	v_pk_mul_f32 v[36:37], v[40:41], v[38:39] op_sel_hi:[0,1]
	v_pk_mul_f32 v[8:9], v[8:9], v[36:37]
	global_load_dwordx4 v[36:39], v41, s[8:9] offset:192
	v_cvt_pk_bf16_f32 v4, v6, v7
	v_cvt_pk_bf16_f32 v5, v8, v9
	s_waitcnt vmcnt(0)
	v_pk_mul_f32 v[36:37], v[40:41], v[36:37] op_sel_hi:[0,1]
	v_pk_mul_f32 v[10:11], v[10:11], v[36:37]
	v_pk_mul_f32 v[36:37], v[40:41], v[38:39] op_sel_hi:[0,1]
	v_pk_mul_f32 v[12:13], v[12:13], v[36:37]
	global_load_dwordx4 v[36:39], v41, s[8:9] offset:224
	s_waitcnt vmcnt(0)
	v_pk_mul_f32 v[36:37], v[40:41], v[36:37] op_sel_hi:[0,1]
	v_pk_mul_f32 v[14:15], v[14:15], v[36:37]
	v_pk_mul_f32 v[36:37], v[40:41], v[38:39] op_sel_hi:[0,1]
	v_pk_mul_f32 v[16:17], v[16:17], v[36:37]
	global_load_dwordx4 v[36:39], v41, s[8:9]
	s_waitcnt vmcnt(0)
	v_pk_mul_f32 v[36:37], v[40:41], v[36:37] op_sel_hi:[0,1]
	v_pk_mul_f32 v[24:25], v[24:25], v[36:37]
	v_pk_mul_f32 v[36:37], v[40:41], v[38:39] op_sel_hi:[0,1]
	v_pk_mul_f32 v[26:27], v[26:27], v[36:37]
	global_load_dwordx4 v[36:39], v41, s[8:9] offset:32
	v_cvt_pk_bf16_f32 v24, v24, v25
	v_cvt_pk_bf16_f32 v25, v26, v27
	s_waitcnt vmcnt(0)
	v_pk_mul_f32 v[36:37], v[40:41], v[36:37] op_sel_hi:[0,1]
	v_pk_mul_f32 v[28:29], v[28:29], v[36:37]
	v_pk_mul_f32 v[36:37], v[40:41], v[38:39] op_sel_hi:[0,1]
	v_pk_mul_f32 v[30:31], v[30:31], v[36:37]
	global_load_dwordx4 v[36:39], v41, s[8:9] offset:64
	s_waitcnt vmcnt(0)
	v_pk_mul_f32 v[36:37], v[40:41], v[36:37] op_sel_hi:[0,1]
	v_pk_mul_f32 v[32:33], v[32:33], v[36:37]
	v_pk_mul_f32 v[36:37], v[40:41], v[38:39] op_sel_hi:[0,1]
	v_pk_mul_f32 v[34:35], v[34:35], v[36:37]
	global_load_dwordx4 v[36:39], v41, s[8:9] offset:96
	s_nop 0
	global_store_dwordx2 v[18:19], v[24:25], off offset:1024
	global_store_dwordx2 v[18:19], v[2:3], off offset:1088
	v_cvt_pk_bf16_f32 v2, v28, v29
	v_cvt_pk_bf16_f32 v3, v30, v31
	global_store_dwordx2 v[18:19], v[2:3], off offset:1040
	global_store_dwordx2 v[18:19], v[4:5], off offset:1104
	v_cvt_pk_bf16_f32 v2, v32, v33
	v_cvt_pk_bf16_f32 v3, v34, v35
	v_cvt_pk_bf16_f32 v4, v10, v11
	v_cvt_pk_bf16_f32 v5, v12, v13
	global_store_dwordx2 v[18:19], v[2:3], off offset:1056
	global_store_dwordx2 v[18:19], v[4:5], off offset:1120
	v_cvt_pk_bf16_f32 v4, v14, v15
	v_cvt_pk_bf16_f32 v5, v16, v17
	s_waitcnt vmcnt(6)
	v_pk_mul_f32 v[36:37], v[40:41], v[36:37] op_sel_hi:[0,1]
	v_pk_mul_f32 v[20:21], v[20:21], v[36:37]
	v_pk_mul_f32 v[36:37], v[40:41], v[38:39] op_sel_hi:[0,1]
	v_pk_mul_f32 v[22:23], v[22:23], v[36:37]
	v_cvt_pk_bf16_f32 v2, v20, v21
	v_cvt_pk_bf16_f32 v3, v22, v23
	global_store_dwordx2 v[18:19], v[2:3], off offset:1072
	global_store_dwordx2 v[18:19], v[4:5], off offset:1136
	s_branch .LBB0_951
